# SB step control trims (DMA issue without m0 save/restore, short all-done / wave-done tests) + NSA lean step: ring base in s98
# baseline (speedup 1.0000x reference)
.LBB0_532:
	s_and_b32 s17, s45, 8
	v_lshl_add_u32 v3, s17, 2, v165
	ds_read_b32 v3, v3
	s_waitcnt lgkmcnt(0)
	v_cmp_eq_u32_e32 vcc, 0, v3
	s_mov_b64 s[18:19], -1
	s_nop 0
	s_cbranch_vccz .LBB0_517
	s_branch .LBB0_536
.LBB0_533:
	s_and_b64 vcc, exec, s[18:19]
	s_cbranch_vccz .LBB0_531
	s_waitcnt vmcnt(8) lgkmcnt(0)
	s_barrier
	s_cmp_eq_u32 s43, 5
	s_cbranch_scc0 .LBB0_532

.LBB0_536:
	s_cmp_ge_u32 s43, s36
	s_cbranch_scc1 .LBB0_538
	s_mul_hi_u32 s17, s43, 0xaaaaaaab
	s_lshr_b32 s17, s17, 2
	s_mul_i32 s17, s17, 0x18000
	s_sub_i32 s47, s29, s17
	s_ashr_i32 s17, s16, 31
	s_lshl_b64 s[18:19], s[16:17], 13
	s_add_i32 m0, s44, s47
	v_lshl_add_u64 v[38:39], v[120:121], 0, s[18:19]
	v_lshl_add_u64 v[86:87], v[122:123], 0, s[18:19]
	global_load_lds_dwordx4 v[38:39], off
	s_add_i32 m0, m0, 0x2000
	s_nop 0
	global_load_lds_dwordx4 v[86:87], off
.LBB0_538:
	s_and_b64 vcc, exec, s[4:5]
	s_mov_b64 s[4:5], -1
	s_cbranch_vccnz .LBB0_545
	s_cmp_gt_i32 s41, s37
	s_mov_b64 s[4:5], 0
	s_cbranch_scc1 .LBB0_545
	s_mul_hi_u32 s4, s46, 0xaaaaaaab
	s_lshr_b32 s17, s4, 2
	s_mul_i32 s17, s17, 0x18000
	v_subrev_u32_e32 v3, s17, v185
	s_add_i32 s4, s44, 0
	v_add_u32_e32 v3, s4, v3
	ds_read_b128 v[38:41], v3
	ds_read_b128 v[42:45], v3 offset:512
	ds_read_b128 v[86:89], v3 offset:2048
	ds_read_b128 v[90:93], v3 offset:2560
	s_add_i32 s18, s41, 63
	s_waitcnt lgkmcnt(3)
	v_mfma_f32_32x32x16_bf16 v[54:69], v[38:41], v[82:85], 0
	s_mov_b64 s[4:5], -1
	s_cmp_lt_i32 s18, s34
	s_waitcnt lgkmcnt(2)
	v_mfma_f32_32x32x16_bf16 v[38:53], v[42:45], v[82:85], 0
	s_waitcnt lgkmcnt(1)
	v_mfma_f32_32x32x16_bf16 v[54:69], v[86:89], v[78:81], v[54:69]
	s_waitcnt lgkmcnt(0)
	v_mfma_f32_32x32x16_bf16 v[38:53], v[90:93], v[78:81], v[38:53]
	ds_read_b128 v[86:89], v3 offset:4096
	ds_read_b128 v[90:93], v3 offset:4608
	s_waitcnt lgkmcnt(1)
	v_mfma_f32_32x32x16_bf16 v[54:69], v[86:89], v[74:77], v[54:69]
	s_waitcnt lgkmcnt(0)
	v_mfma_f32_32x32x16_bf16 v[38:53], v[90:93], v[74:77], v[38:53]
	ds_read_b128 v[86:89], v3 offset:6144
	ds_read_b128 v[90:93], v3 offset:6656
	s_waitcnt lgkmcnt(1)
	v_mfma_f32_32x32x16_bf16 v[54:69], v[86:89], v[70:73], v[54:69]
	s_waitcnt lgkmcnt(0)
	v_mfma_f32_32x32x16_bf16 v[38:53], v[90:93], v[70:73], v[38:53]
	s_nop 9
	v_exp_f32_e64 v247, -|v54|
	v_exp_f32_e64 v246, -|v55|
	v_exp_f32_e64 v239, -|v56|
	v_exp_f32_e64 v238, -|v57|
	v_exp_f32_e64 v231, -|v58|
	v_exp_f32_e64 v230, -|v59|
	v_exp_f32_e64 v223, -|v60|
	v_exp_f32_e64 v243, -|v38|
	v_exp_f32_e64 v242, -|v39|
	v_exp_f32_e64 v235, -|v40|
	v_exp_f32_e64 v234, -|v41|
	v_exp_f32_e64 v227, -|v42|
	v_exp_f32_e64 v226, -|v43|
	v_exp_f32_e64 v222, -|v61|
	v_exp_f32_e64 v219, -|v44|
	v_exp_f32_e64 v218, -|v45|
	v_exp_f32_e64 v215, -|v62|
	v_exp_f32_e64 v213, -|v63|
	v_exp_f32_e64 v211, -|v46|
	v_exp_f32_e64 v210, -|v47|
	v_exp_f32_e64 v207, -|v64|
	v_exp_f32_e64 v206, -|v65|
	v_exp_f32_e64 v203, -|v48|
	v_exp_f32_e64 v202, -|v49|
	v_exp_f32_e64 v199, -|v66|
	v_exp_f32_e64 v198, -|v67|
	v_exp_f32_e64 v195, -|v50|
	v_exp_f32_e64 v194, -|v51|
	v_exp_f32_e64 v190, -|v68|
	v_exp_f32_e64 v189, -|v69|
	v_exp_f32_e64 v187, -|v52|
	v_exp_f32_e64 v186, -|v53|
	s_cbranch_scc1 .LBB0_542
	v_add_f32_e32 v86, 1.0, v247
	v_add_f32_e32 v87, 1.0, v246
	v_log_f32_e32 v86, v86
	v_log_f32_e32 v87, v87
	v_max_f32_e32 v88, 0, v54
	v_max_f32_e32 v89, 0, v55
	v_cmp_lt_i32_e32 vcc, 0, v184
	v_pk_add_f32 v[86:87], v[88:89], v[86:87]
	v_cmp_lt_i32_e64 s[4:5], 1, v184
	v_pk_add_f32 v[88:89], v[54:55], v[86:87] neg_lo:[0,1] neg_hi:[0,1]
	v_cndmask_b32_e32 v86, 0, v86, vcc
	v_cndmask_b32_e64 v87, 0, v87, s[4:5]
	v_and_b32_e32 v91, 0xffff0000, v87
	v_and_b32_e32 v90, 0xffff0000, v86
	v_cndmask_b32_e32 v124, v161, v88, vcc
	v_cndmask_b32_e64 v125, v161, v89, s[4:5]
	v_pk_add_f32 v[88:89], v[86:87], 0 op_sel_hi:[1,0]
	v_or_b32_sdwa v98, v91, v86 dst_sel:DWORD dst_unused:UNUSED_PAD src0_sel:DWORD src1_sel:WORD_1
	v_pk_add_f32 v[86:87], v[86:87], v[90:91] neg_lo:[0,1] neg_hi:[0,1]
	v_add_f32_e32 v90, 1.0, v243
	v_add_f32_e32 v91, 1.0, v242
	v_log_f32_e32 v90, v90
	v_log_f32_e32 v91, v91
	v_cvt_pk_bf16_f32 v94, v86, v87
	v_max_f32_e32 v86, 0, v38
	v_max_f32_e32 v87, 0, v39
	v_pk_add_f32 v[86:87], v[86:87], v[90:91]
	v_cmp_lt_i32_e32 vcc, 32, v184
	v_pk_add_f32 v[90:91], v[38:39], v[86:87] neg_lo:[0,1] neg_hi:[0,1]
	v_cmp_lt_i32_e64 s[4:5], 33, v184
	v_cndmask_b32_e32 v126, v161, v90, vcc
	v_cndmask_b32_e32 v90, 0, v86, vcc
	v_cndmask_b32_e64 v127, v161, v91, s[4:5]
	v_cndmask_b32_e64 v91, 0, v87, s[4:5]
	v_and_b32_e32 v93, 0xffff0000, v91
	v_and_b32_e32 v92, 0xffff0000, v90
	v_add_f32_e32 v87, 1.0, v239
	v_pk_add_f32 v[88:89], v[90:91], v[88:89]
	v_or_b32_sdwa v86, v93, v90 dst_sel:DWORD dst_unused:UNUSED_PAD src0_sel:DWORD src1_sel:WORD_1
	v_pk_add_f32 v[90:91], v[90:91], v[92:93] neg_lo:[0,1] neg_hi:[0,1]
	v_log_f32_e32 v92, v87
	v_add_f32_e32 v87, 1.0, v238
	v_log_f32_e32 v93, v87
	v_max_f32_e32 v96, 0, v56
	v_max_f32_e32 v97, 0, v57
	v_cmp_lt_i32_e32 vcc, 2, v184
	v_pk_add_f32 v[92:93], v[96:97], v[92:93]
	v_cmp_lt_i32_e64 s[4:5], 3, v184
	v_pk_add_f32 v[96:97], v[56:57], v[92:93] neg_lo:[0,1] neg_hi:[0,1]
	v_cndmask_b32_e32 v92, 0, v92, vcc
	v_cndmask_b32_e64 v93, 0, v93, s[4:5]
	v_cndmask_b32_e32 v128, v161, v96, vcc
	v_cndmask_b32_e64 v129, v161, v97, s[4:5]
	v_and_b32_e32 v97, 0xffff0000, v93
	v_and_b32_e32 v96, 0xffff0000, v92
	v_add_f32_e32 v87, 1.0, v235
	v_pk_add_f32 v[88:89], v[92:93], v[88:89]
	v_or_b32_sdwa v99, v97, v92 dst_sel:DWORD dst_unused:UNUSED_PAD src0_sel:DWORD src1_sel:WORD_1
	v_pk_add_f32 v[92:93], v[92:93], v[96:97] neg_lo:[0,1] neg_hi:[0,1]
	v_log_f32_e32 v96, v87
	v_add_f32_e32 v87, 1.0, v234
	v_log_f32_e32 v97, v87
	v_cvt_pk_bf16_f32 v95, v92, v93
	v_max_f32_e32 v92, 0, v40
	v_max_f32_e32 v93, 0, v41
	v_pk_add_f32 v[92:93], v[92:93], v[96:97]
	v_cmp_lt_i32_e32 vcc, 34, v184
	v_cmp_lt_i32_e64 s[4:5], 35, v184
	v_pk_add_f32 v[96:97], v[40:41], v[92:93] neg_lo:[0,1] neg_hi:[0,1]
	v_cndmask_b32_e32 v92, 0, v92, vcc
	v_cndmask_b32_e64 v93, 0, v93, s[4:5]
	v_cvt_pk_bf16_f32 v90, v90, v91
	v_cndmask_b32_e32 v130, v161, v96, vcc
	v_cndmask_b32_e64 v131, v161, v97, s[4:5]
	v_and_b32_e32 v97, 0xffff0000, v93
	v_and_b32_e32 v96, 0xffff0000, v92
	v_add_f32_e32 v91, 1.0, v231
	v_pk_add_f32 v[88:89], v[92:93], v[88:89]
	v_or_b32_sdwa v87, v97, v92 dst_sel:DWORD dst_unused:UNUSED_PAD src0_sel:DWORD src1_sel:WORD_1
	v_pk_add_f32 v[92:93], v[92:93], v[96:97] neg_lo:[0,1] neg_hi:[0,1]
	v_log_f32_e32 v96, v91
	v_add_f32_e32 v91, 1.0, v230
	v_log_f32_e32 v97, v91
	v_cvt_pk_bf16_f32 v91, v92, v93
	v_max_f32_e32 v92, 0, v58
	v_max_f32_e32 v93, 0, v59
	v_pk_add_f32 v[92:93], v[92:93], v[96:97]
	v_cmp_lt_i32_e32 vcc, 8, v184
	v_cmp_lt_i32_e64 s[4:5], 9, v184
	v_pk_add_f32 v[96:97], v[58:59], v[92:93] neg_lo:[0,1] neg_hi:[0,1]
	v_cndmask_b32_e32 v92, 0, v92, vcc
	v_cndmask_b32_e64 v93, 0, v93, s[4:5]
	v_cndmask_b32_e32 v132, v161, v96, vcc
	v_cndmask_b32_e64 v133, v161, v97, s[4:5]
	v_and_b32_e32 v97, 0xffff0000, v93
	v_and_b32_e32 v96, 0xffff0000, v92
	v_pk_add_f32 v[88:89], v[92:93], v[88:89]
	v_or_b32_sdwa v100, v97, v92 dst_sel:DWORD dst_unused:UNUSED_PAD src0_sel:DWORD src1_sel:WORD_1
	v_pk_add_f32 v[92:93], v[92:93], v[96:97] neg_lo:[0,1] neg_hi:[0,1]
	v_add_f32_e32 v96, 1.0, v227
	v_log_f32_e32 v102, v96
	v_add_f32_e32 v96, 1.0, v226
	v_log_f32_e32 v103, v96
	v_cvt_pk_bf16_f32 v96, v92, v93
	v_max_f32_e32 v92, 0, v42
	v_max_f32_e32 v93, 0, v43
	v_pk_add_f32 v[92:93], v[92:93], v[102:103]
	v_cmp_lt_i32_e32 vcc, 40, v184
	v_cmp_lt_i32_e64 s[4:5], 41, v184
	v_pk_add_f32 v[102:103], v[42:43], v[92:93] neg_lo:[0,1] neg_hi:[0,1]
	v_cndmask_b32_e32 v92, 0, v92, vcc
	v_cndmask_b32_e64 v93, 0, v93, s[4:5]
	v_cndmask_b32_e32 v134, v161, v102, vcc
	v_cndmask_b32_e64 v135, v161, v103, s[4:5]
	v_pk_add_f32 v[102:103], v[92:93], v[88:89]
	v_and_b32_e32 v105, 0xffff0000, v93
	v_and_b32_e32 v104, 0xffff0000, v92
	v_add_f32_e32 v89, 1.0, v223
	v_or_b32_sdwa v88, v105, v92 dst_sel:DWORD dst_unused:UNUSED_PAD src0_sel:DWORD src1_sel:WORD_1
	v_pk_add_f32 v[92:93], v[92:93], v[104:105] neg_lo:[0,1] neg_hi:[0,1]
	v_log_f32_e32 v104, v89
	v_add_f32_e32 v89, 1.0, v222
	v_log_f32_e32 v105, v89
	v_max_f32_e32 v106, 0, v60
	v_max_f32_e32 v107, 0, v61
	v_cmp_lt_i32_e32 vcc, 10, v184
	v_pk_add_f32 v[104:105], v[106:107], v[104:105]
	v_cmp_lt_i32_e64 s[4:5], 11, v184
	v_pk_add_f32 v[106:107], v[60:61], v[104:105] neg_lo:[0,1] neg_hi:[0,1]
	v_cndmask_b32_e32 v104, 0, v104, vcc
	v_cndmask_b32_e64 v105, 0, v105, s[4:5]
	v_cndmask_b32_e32 v136, v161, v106, vcc
	v_cndmask_b32_e64 v137, v161, v107, s[4:5]
	v_and_b32_e32 v107, 0xffff0000, v105
	v_and_b32_e32 v106, 0xffff0000, v104
	v_add_f32_e32 v89, 1.0, v219
	v_pk_add_f32 v[102:103], v[104:105], v[102:103]
	v_or_b32_sdwa v101, v107, v104 dst_sel:DWORD dst_unused:UNUSED_PAD src0_sel:DWORD src1_sel:WORD_1
	v_pk_add_f32 v[104:105], v[104:105], v[106:107] neg_lo:[0,1] neg_hi:[0,1]
	v_log_f32_e32 v106, v89
	v_add_f32_e32 v89, 1.0, v218
	v_log_f32_e32 v107, v89
	v_cvt_pk_bf16_f32 v97, v104, v105
	v_max_f32_e32 v104, 0, v44
	v_max_f32_e32 v105, 0, v45
	v_pk_add_f32 v[104:105], v[104:105], v[106:107]
	v_cmp_lt_i32_e32 vcc, 42, v184
	v_cmp_lt_i32_e64 s[4:5], 43, v184
	v_pk_add_f32 v[106:107], v[44:45], v[104:105] neg_lo:[0,1] neg_hi:[0,1]
	v_cndmask_b32_e32 v104, 0, v104, vcc
	v_cndmask_b32_e64 v105, 0, v105, s[4:5]
	v_cvt_pk_bf16_f32 v92, v92, v93
	v_cndmask_b32_e32 v138, v161, v106, vcc
	v_cndmask_b32_e64 v139, v161, v107, s[4:5]
	v_and_b32_e32 v107, 0xffff0000, v105
	v_and_b32_e32 v106, 0xffff0000, v104
	v_add_f32_e32 v93, 1.0, v215
	v_pk_add_f32 v[102:103], v[104:105], v[102:103]
	v_or_b32_sdwa v89, v107, v104 dst_sel:DWORD dst_unused:UNUSED_PAD src0_sel:DWORD src1_sel:WORD_1
	v_pk_add_f32 v[104:105], v[104:105], v[106:107] neg_lo:[0,1] neg_hi:[0,1]
	v_log_f32_e32 v106, v93
	v_add_f32_e32 v93, 1.0, v213
	v_log_f32_e32 v107, v93
	v_cvt_pk_bf16_f32 v93, v104, v105
	v_max_f32_e32 v104, 0, v62
	v_max_f32_e32 v105, 0, v63
	v_pk_add_f32 v[104:105], v[104:105], v[106:107]
	v_cmp_lt_i32_e32 vcc, 16, v184
	v_cmp_lt_i32_e64 s[4:5], 17, v184
	v_pk_add_f32 v[106:107], v[62:63], v[104:105] neg_lo:[0,1] neg_hi:[0,1]
	v_cndmask_b32_e32 v104, 0, v104, vcc
	v_cndmask_b32_e64 v105, 0, v105, s[4:5]
	v_cndmask_b32_e32 v140, v161, v106, vcc
	v_cndmask_b32_e64 v141, v161, v107, s[4:5]
	v_and_b32_e32 v107, 0xffff0000, v105
	v_and_b32_e32 v106, 0xffff0000, v104
	v_pk_add_f32 v[102:103], v[104:105], v[102:103]
	v_or_b32_sdwa v110, v107, v104 dst_sel:DWORD dst_unused:UNUSED_PAD src0_sel:DWORD src1_sel:WORD_1
	v_pk_add_f32 v[104:105], v[104:105], v[106:107] neg_lo:[0,1] neg_hi:[0,1]
	v_add_f32_e32 v106, 1.0, v211
	v_add_f32_e32 v107, 1.0, v210
	v_log_f32_e32 v106, v106
	v_log_f32_e32 v107, v107
	v_cvt_pk_bf16_f32 v114, v104, v105
	v_max_f32_e32 v104, 0, v46
	v_max_f32_e32 v105, 0, v47
	v_pk_add_f32 v[104:105], v[104:105], v[106:107]
	v_cmp_lt_i32_e32 vcc, 48, v184
	v_cmp_lt_i32_e64 s[4:5], 49, v184
	v_pk_add_f32 v[106:107], v[46:47], v[104:105] neg_lo:[0,1] neg_hi:[0,1]
	v_cndmask_b32_e32 v104, 0, v104, vcc
	v_cndmask_b32_e64 v105, 0, v105, s[4:5]
	v_pk_add_f32 v[108:109], v[104:105], v[102:103]
	v_and_b32_e32 v103, 0xffff0000, v105
	v_and_b32_e32 v102, 0xffff0000, v104
	v_cndmask_b32_e32 v144, v161, v106, vcc
	v_or_b32_sdwa v106, v103, v104 dst_sel:DWORD dst_unused:UNUSED_PAD src0_sel:DWORD src1_sel:WORD_1
	v_pk_add_f32 v[102:103], v[104:105], v[102:103] neg_lo:[0,1] neg_hi:[0,1]
	v_add_f32_e32 v104, 1.0, v207
	v_add_f32_e32 v105, 1.0, v206
	v_log_f32_e32 v104, v104
	v_log_f32_e32 v105, v105
	v_max_f32_e32 v112, 0, v64
	v_max_f32_e32 v113, 0, v65
	v_cndmask_b32_e64 v145, v161, v107, s[4:5]
	v_pk_add_f32 v[104:105], v[112:113], v[104:105]
	v_cmp_lt_i32_e32 vcc, 18, v184
	v_cmp_lt_i32_e64 s[4:5], 19, v184
	v_pk_add_f32 v[112:113], v[64:65], v[104:105] neg_lo:[0,1] neg_hi:[0,1]
	v_cndmask_b32_e32 v104, 0, v104, vcc
	v_cndmask_b32_e64 v105, 0, v105, s[4:5]
	v_cvt_pk_bf16_f32 v102, v102, v103
	v_cndmask_b32_e32 v146, v161, v112, vcc
	v_cndmask_b32_e64 v147, v161, v113, s[4:5]
	v_and_b32_e32 v113, 0xffff0000, v105
	v_and_b32_e32 v112, 0xffff0000, v104
	v_add_f32_e32 v103, 1.0, v203
	v_pk_add_f32 v[108:109], v[104:105], v[108:109]
	v_or_b32_sdwa v111, v113, v104 dst_sel:DWORD dst_unused:UNUSED_PAD src0_sel:DWORD src1_sel:WORD_1
	v_pk_add_f32 v[104:105], v[104:105], v[112:113] neg_lo:[0,1] neg_hi:[0,1]
	v_log_f32_e32 v112, v103
	v_add_f32_e32 v103, 1.0, v202
	v_log_f32_e32 v113, v103
	v_cvt_pk_bf16_f32 v115, v104, v105
	v_max_f32_e32 v104, 0, v48
	v_max_f32_e32 v105, 0, v49
	v_pk_add_f32 v[104:105], v[104:105], v[112:113]
	v_cmp_lt_i32_e32 vcc, 50, v184
	v_cmp_lt_i32_e64 s[4:5], 51, v184
	v_pk_add_f32 v[112:113], v[48:49], v[104:105] neg_lo:[0,1] neg_hi:[0,1]
	v_cndmask_b32_e32 v104, 0, v104, vcc
	v_cndmask_b32_e64 v105, 0, v105, s[4:5]
	v_cndmask_b32_e32 v152, v161, v112, vcc
	v_cndmask_b32_e64 v153, v161, v113, s[4:5]
	v_and_b32_e32 v113, 0xffff0000, v105
	v_and_b32_e32 v112, 0xffff0000, v104
	v_add_f32_e32 v103, 1.0, v199
	v_pk_add_f32 v[108:109], v[104:105], v[108:109]
	v_or_b32_sdwa v107, v113, v104 dst_sel:DWORD dst_unused:UNUSED_PAD src0_sel:DWORD src1_sel:WORD_1
	v_pk_add_f32 v[104:105], v[104:105], v[112:113] neg_lo:[0,1] neg_hi:[0,1]
	v_log_f32_e32 v112, v103
	v_add_f32_e32 v103, 1.0, v198
	v_log_f32_e32 v113, v103
	v_cvt_pk_bf16_f32 v103, v104, v105
	v_max_f32_e32 v104, 0, v66
	v_max_f32_e32 v105, 0, v67
	v_pk_add_f32 v[104:105], v[104:105], v[112:113]
	v_cmp_lt_i32_e64 s[4:5], 25, v184
	v_pk_add_f32 v[112:113], v[66:67], v[104:105] neg_lo:[0,1] neg_hi:[0,1]
	v_cmp_lt_i32_e32 vcc, 24, v184
	v_cndmask_b32_e64 v157, v161, v113, s[4:5]
	v_add_f32_e32 v113, 1.0, v195
	v_log_f32_e32 v142, v113
	v_add_f32_e32 v113, 1.0, v194
	v_cndmask_b32_e64 v105, 0, v105, s[4:5]
	v_cndmask_b32_e32 v104, 0, v104, vcc
	v_log_f32_e32 v143, v113
	v_and_b32_e32 v117, 0xffff0000, v105
	v_and_b32_e32 v116, 0xffff0000, v104
	v_cndmask_b32_e32 v156, v161, v112, vcc
	v_pk_add_f32 v[108:109], v[104:105], v[108:109]
	v_or_b32_sdwa v112, v117, v104 dst_sel:DWORD dst_unused:UNUSED_PAD src0_sel:DWORD src1_sel:WORD_1
	v_pk_add_f32 v[104:105], v[104:105], v[116:117] neg_lo:[0,1] neg_hi:[0,1]
	v_cmp_lt_i32_e32 vcc, 56, v184
	v_cvt_pk_bf16_f32 v116, v104, v105
	v_max_f32_e32 v104, 0, v50
	v_max_f32_e32 v105, 0, v51
	v_pk_add_f32 v[104:105], v[104:105], v[142:143]
	v_cmp_lt_i32_e64 s[4:5], 57, v184
	v_pk_add_f32 v[142:143], v[50:51], v[104:105] neg_lo:[0,1] neg_hi:[0,1]
	v_cndmask_b32_e32 v104, 0, v104, vcc
	v_cndmask_b32_e64 v105, 0, v105, s[4:5]
	v_cndmask_b32_e32 v158, v161, v142, vcc
	v_cndmask_b32_e64 v159, v161, v143, s[4:5]
	v_pk_add_f32 v[142:143], v[104:105], v[108:109]
	v_and_b32_e32 v149, 0xffff0000, v105
	v_and_b32_e32 v148, 0xffff0000, v104
	v_add_f32_e32 v109, 1.0, v190
	v_or_b32_sdwa v108, v149, v104 dst_sel:DWORD dst_unused:UNUSED_PAD src0_sel:DWORD src1_sel:WORD_1
	v_pk_add_f32 v[104:105], v[104:105], v[148:149] neg_lo:[0,1] neg_hi:[0,1]
	v_log_f32_e32 v148, v109
	v_add_f32_e32 v109, 1.0, v189
	v_log_f32_e32 v149, v109
	v_max_f32_e32 v150, 0, v68
	v_max_f32_e32 v151, 0, v69
	v_cmp_lt_i32_e32 vcc, 26, v184
	v_pk_add_f32 v[148:149], v[150:151], v[148:149]
	v_cmp_lt_i32_e64 s[4:5], 27, v184
	v_pk_add_f32 v[150:151], v[68:69], v[148:149] neg_lo:[0,1] neg_hi:[0,1]
	v_cndmask_b32_e32 v148, 0, v148, vcc
	v_cndmask_b32_e64 v149, 0, v149, s[4:5]
	v_cvt_pk_bf16_f32 v104, v104, v105
	v_cndmask_b32_e32 v154, v161, v150, vcc
	v_cndmask_b32_e64 v155, v161, v151, s[4:5]
	v_and_b32_e32 v151, 0xffff0000, v149
	v_and_b32_e32 v150, 0xffff0000, v148
	v_add_f32_e32 v105, 1.0, v187
	v_pk_add_f32 v[142:143], v[148:149], v[142:143]
	v_or_b32_sdwa v113, v151, v148 dst_sel:DWORD dst_unused:UNUSED_PAD src0_sel:DWORD src1_sel:WORD_1
	v_pk_add_f32 v[148:149], v[148:149], v[150:151] neg_lo:[0,1] neg_hi:[0,1]
	v_log_f32_e32 v150, v105
	v_add_f32_e32 v105, 1.0, v186
	v_log_f32_e32 v151, v105
	v_cvt_pk_bf16_f32 v117, v148, v149
	v_max_f32_e32 v148, 0, v52
	v_max_f32_e32 v149, 0, v53
	v_pk_add_f32 v[148:149], v[148:149], v[150:151]
	v_cmp_lt_i32_e32 vcc, 58, v184
	v_pk_add_f32 v[150:151], v[52:53], v[148:149] neg_lo:[0,1] neg_hi:[0,1]
	v_cmp_lt_i32_e64 s[4:5], 59, v184
	v_cndmask_b32_e32 v150, v161, v150, vcc
	v_cndmask_b32_e32 v148, 0, v148, vcc
	v_cndmask_b32_e64 v151, v161, v151, s[4:5]
	v_cndmask_b32_e64 v149, 0, v149, s[4:5]
	s_mov_b64 s[4:5], 0

.LBB0_572:
	v_lshlrev_b32_e32 v202, 10, v3
	v_lshlrev_b32_e32 v203, 4, v198
	v_add3_u32 v69, 0, v202, v203
	ds_read_b128 v[4:7], v69
	ds_read_b128 v[8:11], v69 offset:512
	s_mov_b32 s0, 0xf149f2ca
	v_ashrrev_i32_e32 v182, 3, v68
	s_waitcnt lgkmcnt(1)
	v_mfma_f32_32x32x16_bf16 v[52:67], v[4:7], v[158:161], 0
	s_cmp_lt_i32 s82, 0
	s_waitcnt lgkmcnt(0)
	v_mfma_f32_32x32x16_bf16 v[36:51], v[8:11], v[158:161], 0
	ds_read_b128 v[4:7], v69 offset:2048
	ds_read_b128 v[8:11], v69 offset:2560
	s_waitcnt lgkmcnt(1)
	v_mfma_f32_32x32x16_bf16 v[52:67], v[4:7], v[154:157], v[52:67]
	s_waitcnt lgkmcnt(0)
	v_mfma_f32_32x32x16_bf16 v[36:51], v[8:11], v[154:157], v[36:51]
	ds_read_b128 v[4:7], v69 offset:4096
	ds_read_b128 v[8:11], v69 offset:4608
	s_waitcnt lgkmcnt(1)
	v_mfma_f32_32x32x16_bf16 v[52:67], v[4:7], v[150:153], v[52:67]
	s_waitcnt lgkmcnt(0)
	v_mfma_f32_32x32x16_bf16 v[36:51], v[8:11], v[150:153], v[36:51]
	ds_read_b128 v[4:7], v69 offset:6144
	ds_read_b128 v[8:11], v69 offset:6656
	s_waitcnt lgkmcnt(1)
	v_mfma_f32_32x32x16_bf16 v[52:67], v[4:7], v[146:149], v[52:67]
	s_waitcnt lgkmcnt(0)
	v_mfma_f32_32x32x16_bf16 v[36:51], v[8:11], v[146:149], v[36:51]
	ds_read_b128 v[4:7], v69 offset:16384
	ds_read_b128 v[8:11], v69 offset:16896
	ds_read_b128 v[74:77], v69 offset:18432
	ds_read_b128 v[78:81], v69 offset:18944
	s_waitcnt lgkmcnt(3)
	v_mfma_f32_32x32x16_bf16 v[20:35], v[4:7], v[158:161], 0
	s_waitcnt lgkmcnt(2)
	v_mfma_f32_32x32x16_bf16 v[4:19], v[8:11], v[158:161], 0
	s_waitcnt lgkmcnt(1)
	v_mfma_f32_32x32x16_bf16 v[20:35], v[74:77], v[154:157], v[20:35]
	s_waitcnt lgkmcnt(0)
	v_mfma_f32_32x32x16_bf16 v[4:19], v[78:81], v[154:157], v[4:19]
	ds_read_b128 v[74:77], v69 offset:20480
	ds_read_b128 v[78:81], v69 offset:20992
	s_waitcnt lgkmcnt(1)
	v_mfma_f32_32x32x16_bf16 v[20:35], v[74:77], v[150:153], v[20:35]
	s_waitcnt lgkmcnt(0)
	v_mfma_f32_32x32x16_bf16 v[4:19], v[78:81], v[150:153], v[4:19]
	ds_read_b128 v[74:77], v69 offset:22528
	ds_read_b128 v[78:81], v69 offset:23040
	v_lshlrev_b32_e32 v69, 6, v3
	v_sub_u32_e32 v69, v72, v69
	v_subrev_u32_e32 v72, 31, v69
	v_cmp_lt_i32_e32 vcc, -1, v72
	s_nop 1
	v_cndmask_b32_e32 v52, v195, v52, vcc
	v_cmp_lt_i32_e32 vcc, 15, v72
	s_waitcnt lgkmcnt(1)
	v_mfma_f32_32x32x16_bf16 v[20:35], v[74:77], v[146:149], v[20:35]
	v_cndmask_b32_e32 v53, v195, v53, vcc
	v_cmp_lt_i32_e32 vcc, 31, v72
	v_max3_f32 v69, v52, s0, v53
	s_movk_i32 s0, 0x7f
	v_cndmask_b32_e32 v54, v195, v54, vcc
	v_cmp_lt_i32_e32 vcc, 47, v72
	s_waitcnt lgkmcnt(0)
	v_mfma_f32_32x32x16_bf16 v[4:19], v[78:81], v[146:149], v[4:19]
	v_cndmask_b32_e32 v55, v195, v55, vcc
	v_cmp_lt_i32_e32 vcc, s0, v72
	s_movk_i32 s0, 0x8f
	v_max3_f32 v69, v69, v54, v55
	v_cndmask_b32_e32 v73, v195, v56, vcc
	v_cmp_lt_i32_e32 vcc, s0, v72
	s_movk_i32 s0, 0x9f
	s_nop 0
	v_cndmask_b32_e32 v74, v195, v57, vcc
	v_cmp_lt_i32_e32 vcc, s0, v72
	s_movk_i32 s0, 0xaf
	v_max3_f32 v56, v69, v73, v74
	v_cndmask_b32_e32 v75, v195, v58, vcc
	v_cmp_lt_i32_e32 vcc, s0, v72
	s_movk_i32 s0, 0xff
	s_nop 0
	v_cndmask_b32_e32 v76, v195, v59, vcc
	v_cmp_lt_i32_e32 vcc, s0, v72
	s_movk_i32 s0, 0x10f
	v_max3_f32 v56, v56, v75, v76
	v_cndmask_b32_e32 v77, v195, v60, vcc
	v_cmp_lt_i32_e32 vcc, s0, v72
	s_movk_i32 s0, 0x11f
	s_nop 0
	v_cndmask_b32_e32 v78, v195, v61, vcc
	v_cmp_lt_i32_e32 vcc, s0, v72
	s_movk_i32 s0, 0x12f
	v_max3_f32 v56, v56, v77, v78
	v_cndmask_b32_e32 v79, v195, v62, vcc
	v_cmp_lt_i32_e32 vcc, s0, v72
	s_movk_i32 s0, 0x17f
	s_nop 0
	v_cndmask_b32_e32 v80, v195, v63, vcc
	v_cmp_lt_i32_e32 vcc, s0, v72
	s_movk_i32 s0, 0x18f
	v_max3_f32 v56, v56, v79, v80
	v_cndmask_b32_e32 v81, v195, v64, vcc
	v_cmp_lt_i32_e32 vcc, s0, v72
	s_movk_i32 s0, 0x19f
	s_nop 0
	v_cndmask_b32_e32 v82, v195, v65, vcc
	v_cmp_lt_i32_e32 vcc, s0, v72
	s_movk_i32 s0, 0x1af
	v_max3_f32 v56, v56, v81, v82
	v_cndmask_b32_e32 v83, v195, v66, vcc
	v_cmp_lt_i32_e32 vcc, s0, v72
	s_movk_i32 s0, 0x1ff
	s_nop 0
	v_cndmask_b32_e32 v84, v195, v67, vcc
	v_cmp_lt_i32_e32 vcc, s0, v72
	s_movk_i32 s0, 0x20f
	v_max3_f32 v56, v56, v83, v84
	v_cndmask_b32_e32 v36, v195, v36, vcc
	v_cmp_lt_i32_e32 vcc, s0, v72
	s_movk_i32 s0, 0x21f
	s_nop 0
	v_cndmask_b32_e32 v37, v195, v37, vcc
	v_cmp_lt_i32_e32 vcc, s0, v72
	s_movk_i32 s0, 0x22f
	v_max3_f32 v56, v56, v36, v37
	v_cndmask_b32_e32 v38, v195, v38, vcc
	v_cmp_lt_i32_e32 vcc, s0, v72
	s_movk_i32 s0, 0x27f
	s_nop 0
	v_cndmask_b32_e32 v39, v195, v39, vcc
	v_cmp_lt_i32_e32 vcc, s0, v72
	s_movk_i32 s0, 0x28f
	v_max3_f32 v56, v56, v38, v39
	v_cndmask_b32_e32 v40, v195, v40, vcc
	v_cmp_lt_i32_e32 vcc, s0, v72
	s_movk_i32 s0, 0x29f
	s_nop 0
	v_cndmask_b32_e32 v41, v195, v41, vcc
	v_cmp_lt_i32_e32 vcc, s0, v72
	s_movk_i32 s0, 0x2af
	v_max3_f32 v56, v56, v40, v41
	v_cndmask_b32_e32 v42, v195, v42, vcc
	v_cmp_lt_i32_e32 vcc, s0, v72
	s_movk_i32 s0, 0x2ff
	s_nop 0
	v_cndmask_b32_e32 v43, v195, v43, vcc
	v_cmp_lt_i32_e32 vcc, s0, v72
	s_movk_i32 s0, 0x30f
	v_max3_f32 v56, v56, v42, v43
	v_cndmask_b32_e32 v44, v195, v44, vcc
	v_cmp_lt_i32_e32 vcc, s0, v72
	s_movk_i32 s0, 0x31f
	s_nop 0
	v_cndmask_b32_e32 v45, v195, v45, vcc
	v_cmp_lt_i32_e32 vcc, s0, v72
	s_movk_i32 s0, 0x32f
	v_max3_f32 v56, v56, v44, v45
	v_cndmask_b32_e32 v46, v195, v46, vcc
	v_cmp_lt_i32_e32 vcc, s0, v72
	s_movk_i32 s0, 0x37f
	s_nop 0
	v_cndmask_b32_e32 v47, v195, v47, vcc
	v_cmp_lt_i32_e32 vcc, s0, v72
	s_movk_i32 s0, 0x38f
	v_max3_f32 v56, v56, v46, v47
	v_cndmask_b32_e32 v48, v195, v48, vcc
	v_cmp_lt_i32_e32 vcc, s0, v72
	s_movk_i32 s0, 0x39f
	s_nop 0
	v_cndmask_b32_e32 v49, v195, v49, vcc
	v_cmp_lt_i32_e32 vcc, s0, v72
	s_movk_i32 s0, 0x3af
	v_max3_f32 v56, v56, v48, v49
	v_cndmask_b32_e32 v50, v195, v50, vcc
	v_cmp_lt_i32_e32 vcc, s0, v72
	s_movk_i32 s0, 0x40f
	s_nop 0
	v_cndmask_b32_e32 v51, v195, v51, vcc
	v_cmp_lt_i32_e32 vcc, s39, v72
	v_max3_f32 v56, v56, v50, v51
	s_nop 0
	v_cndmask_b32_e32 v85, v195, v20, vcc
	v_cmp_lt_i32_e32 vcc, s0, v72
	s_movk_i32 s0, 0x41f
	s_nop 0
	v_cndmask_b32_e32 v86, v195, v21, vcc
	v_cmp_lt_i32_e32 vcc, s0, v72
	s_movk_i32 s0, 0x42f
	v_max3_f32 v20, v56, v85, v86
	v_cndmask_b32_e32 v87, v195, v22, vcc
	v_cmp_lt_i32_e32 vcc, s0, v72
	s_movk_i32 s0, 0x47f
	s_nop 0
	v_cndmask_b32_e32 v88, v195, v23, vcc
	v_cmp_lt_i32_e32 vcc, s0, v72
	s_movk_i32 s0, 0x48f
	v_max3_f32 v20, v20, v87, v88
	v_cndmask_b32_e32 v89, v195, v24, vcc
	v_cmp_lt_i32_e32 vcc, s0, v72
	s_movk_i32 s0, 0x49f
	s_nop 0
	v_cndmask_b32_e32 v90, v195, v25, vcc
	v_cmp_lt_i32_e32 vcc, s0, v72
	s_movk_i32 s0, 0x4af
	v_max3_f32 v20, v20, v89, v90
	v_cndmask_b32_e32 v91, v195, v26, vcc
	v_cmp_lt_i32_e32 vcc, s0, v72
	s_movk_i32 s0, 0x4ff
	s_nop 0
	v_cndmask_b32_e32 v92, v195, v27, vcc
	v_cmp_lt_i32_e32 vcc, s0, v72
	s_movk_i32 s0, 0x50f
	v_max3_f32 v20, v20, v91, v92
	v_cndmask_b32_e32 v93, v195, v28, vcc
	v_cmp_lt_i32_e32 vcc, s0, v72
	s_movk_i32 s0, 0x51f
	s_nop 0
	v_cndmask_b32_e32 v94, v195, v29, vcc
	v_cmp_lt_i32_e32 vcc, s0, v72
	s_movk_i32 s0, 0x52f
	v_max3_f32 v20, v20, v93, v94
	v_cndmask_b32_e32 v95, v195, v30, vcc
	v_cmp_lt_i32_e32 vcc, s0, v72
	s_movk_i32 s0, 0x57f
	s_nop 0
	v_cndmask_b32_e32 v96, v195, v31, vcc
	v_cmp_lt_i32_e32 vcc, s0, v72
	s_movk_i32 s0, 0x58f
	v_max3_f32 v20, v20, v95, v96
	v_cndmask_b32_e32 v97, v195, v32, vcc
	v_cmp_lt_i32_e32 vcc, s0, v72
	s_movk_i32 s0, 0x59f
	s_nop 0
	v_cndmask_b32_e32 v98, v195, v33, vcc
	v_cmp_lt_i32_e32 vcc, s0, v72
	s_movk_i32 s0, 0x5af
	v_max3_f32 v20, v20, v97, v98
	v_cndmask_b32_e32 v99, v195, v34, vcc
	v_cmp_lt_i32_e32 vcc, s0, v72
	s_movk_i32 s0, 0x5ff
	s_nop 0
	v_cndmask_b32_e32 v100, v195, v35, vcc
	v_cmp_lt_i32_e32 vcc, s0, v72
	s_movk_i32 s0, 0x60f
	v_max3_f32 v20, v20, v99, v100
	v_cndmask_b32_e32 v101, v195, v4, vcc
	v_cmp_lt_i32_e32 vcc, s0, v72
	s_movk_i32 s0, 0x61f
	s_nop 0
	v_cndmask_b32_e32 v102, v195, v5, vcc
	v_cmp_lt_i32_e32 vcc, s0, v72
	s_movk_i32 s0, 0x62f
	v_max3_f32 v4, v20, v101, v102
	v_cndmask_b32_e32 v103, v195, v6, vcc
	v_cmp_lt_i32_e32 vcc, s0, v72
	s_movk_i32 s0, 0x67f
	s_nop 0
	v_cndmask_b32_e32 v104, v195, v7, vcc
	v_cmp_lt_i32_e32 vcc, s0, v72
	s_movk_i32 s0, 0x68f
	v_max3_f32 v4, v4, v103, v104
	v_cndmask_b32_e32 v58, v195, v8, vcc
	v_cmp_lt_i32_e32 vcc, s0, v72
	s_movk_i32 s0, 0x69f
	s_nop 0
	v_cndmask_b32_e32 v59, v195, v9, vcc
	v_cmp_lt_i32_e32 vcc, s0, v72
	s_movk_i32 s0, 0x6af
	v_max3_f32 v4, v4, v58, v59
	v_cndmask_b32_e32 v56, v195, v10, vcc
	v_cmp_lt_i32_e32 vcc, s0, v72
	s_movk_i32 s0, 0x6ff
	s_nop 0
	v_cndmask_b32_e32 v57, v195, v11, vcc
	v_cmp_lt_i32_e32 vcc, s0, v72
	s_movk_i32 s0, 0x70f
	v_max3_f32 v4, v4, v56, v57
	v_cndmask_b32_e32 v62, v195, v12, vcc
	v_cmp_lt_i32_e32 vcc, s0, v72
	s_movk_i32 s0, 0x71f
	s_nop 0
	v_cndmask_b32_e32 v63, v195, v13, vcc
	v_cmp_lt_i32_e32 vcc, s0, v72
	s_movk_i32 s0, 0x72f
	v_max3_f32 v4, v4, v62, v63
	v_cndmask_b32_e32 v60, v195, v14, vcc
	v_cmp_lt_i32_e32 vcc, s0, v72
	s_movk_i32 s0, 0x77f
	s_nop 0
	v_cndmask_b32_e32 v61, v195, v15, vcc
	v_cmp_lt_i32_e32 vcc, s0, v72
	s_movk_i32 s0, 0x78f
	v_max3_f32 v4, v4, v60, v61
	v_cndmask_b32_e32 v69, v195, v16, vcc
	v_cmp_lt_i32_e32 vcc, s0, v72
	s_movk_i32 s0, 0x79f
	s_nop 0
	v_cndmask_b32_e32 v66, v195, v17, vcc
	v_cmp_lt_i32_e32 vcc, s0, v72
	s_movk_i32 s0, 0x7af
	v_max3_f32 v4, v4, v69, v66
	v_cndmask_b32_e32 v65, v195, v18, vcc
	v_cmp_lt_i32_e32 vcc, s0, v72
	s_mov_b32 s0, 0xefa18f08
	s_nop 0
	v_cndmask_b32_e32 v64, v195, v19, vcc
	v_max3_f32 v4, v4, v65, v64
	v_mov_b32_e32 v5, v4
	s_nop 1
	v_permlane32_swap_b32_e32 v4, v5
	v_max3_f32 v67, v4, v5, s0
	v_sub_f32_e32 v4, v52, v67
	v_exp_f32_e32 v4, v4
	v_sub_f32_e32 v5, v53, v67
	v_exp_f32_e32 v5, v5
	v_sub_f32_e32 v9, v73, v67
	v_add_f32_e32 v6, 0, v4
	v_exp_f32_e32 v10, v9
	v_add_f32_e32 v7, v5, v6
	v_sub_f32_e32 v6, v54, v67
	v_exp_f32_e32 v6, v6
	v_sub_f32_e32 v9, v74, v67
	v_exp_f32_e32 v11, v9
	v_sub_f32_e32 v13, v77, v67
	v_add_f32_e32 v8, v6, v7
	v_sub_f32_e32 v7, v55, v67
	v_exp_f32_e32 v7, v7
	v_exp_f32_e32 v14, v13
	v_sub_f32_e32 v13, v78, v67
	v_exp_f32_e32 v15, v13
	v_add_f32_e32 v8, v7, v8
	v_add_f32_e32 v8, v10, v8
	v_add_f32_e32 v9, v11, v8
	v_sub_f32_e32 v8, v75, v67
	v_exp_f32_e32 v8, v8
	v_sub_f32_e32 v17, v81, v67
	v_exp_f32_e32 v18, v17
	v_sub_f32_e32 v17, v82, v67
	v_add_f32_e32 v12, v8, v9
	v_sub_f32_e32 v9, v76, v67
	v_exp_f32_e32 v9, v9
	v_exp_f32_e32 v19, v17
	v_sub_f32_e32 v21, v36, v67
	v_exp_f32_e32 v22, v21
	v_add_f32_e32 v12, v9, v12
	v_add_f32_e32 v12, v14, v12
	v_add_f32_e32 v13, v15, v12
	v_sub_f32_e32 v12, v79, v67
	v_exp_f32_e32 v12, v12
	v_sub_f32_e32 v21, v37, v67
	v_exp_f32_e32 v23, v21
	v_sub_f32_e32 v25, v40, v67
	v_add_f32_e32 v16, v12, v13
	v_sub_f32_e32 v13, v80, v67
	v_exp_f32_e32 v13, v13
	v_exp_f32_e32 v26, v25
	v_sub_f32_e32 v25, v41, v67
	v_exp_f32_e32 v27, v25
	v_add_f32_e32 v16, v13, v16
	v_add_f32_e32 v16, v18, v16
	v_add_f32_e32 v17, v19, v16
	v_sub_f32_e32 v16, v83, v67
	v_exp_f32_e32 v16, v16
	v_sub_f32_e32 v29, v44, v67
	v_exp_f32_e32 v30, v29
	v_sub_f32_e32 v29, v45, v67
	v_add_f32_e32 v20, v16, v17
	v_sub_f32_e32 v17, v84, v67
	v_exp_f32_e32 v17, v17
	v_exp_f32_e32 v31, v29
	v_sub_f32_e32 v33, v48, v67
	v_exp_f32_e32 v34, v33
	v_add_f32_e32 v20, v17, v20
	v_add_f32_e32 v20, v22, v20
	v_add_f32_e32 v21, v23, v20
	v_sub_f32_e32 v20, v38, v67
	v_exp_f32_e32 v20, v20
	v_sub_f32_e32 v33, v49, v67
	v_exp_f32_e32 v35, v33
	v_sub_f32_e32 v37, v85, v67
	v_add_f32_e32 v24, v20, v21
	v_sub_f32_e32 v21, v39, v67
	v_exp_f32_e32 v21, v21
	v_exp_f32_e32 v38, v37
	v_sub_f32_e32 v37, v86, v67
	v_exp_f32_e32 v39, v37
	v_add_f32_e32 v24, v21, v24
	v_add_f32_e32 v24, v26, v24
	v_add_f32_e32 v25, v27, v24
	v_sub_f32_e32 v24, v42, v67
	v_exp_f32_e32 v24, v24
	v_sub_f32_e32 v41, v89, v67
	v_exp_f32_e32 v42, v41
	v_sub_f32_e32 v41, v90, v67
	v_add_f32_e32 v28, v24, v25
	v_sub_f32_e32 v25, v43, v67
	v_exp_f32_e32 v25, v25
	v_exp_f32_e32 v43, v41
	v_sub_f32_e32 v45, v93, v67
	v_sub_f32_e32 v49, v97, v67
	v_add_f32_e32 v28, v25, v28
	v_add_f32_e32 v28, v30, v28
	v_add_f32_e32 v29, v31, v28
	v_sub_f32_e32 v28, v46, v67
	v_exp_f32_e32 v28, v28
	v_exp_f32_e32 v46, v45
	v_sub_f32_e32 v45, v94, v67
	v_sub_f32_e32 v53, v101, v67
	v_add_f32_e32 v32, v28, v29
	v_sub_f32_e32 v29, v47, v67
	v_exp_f32_e32 v29, v29
	v_exp_f32_e32 v47, v45
	v_exp_f32_e32 v54, v53
	v_sub_f32_e32 v53, v102, v67
	v_add_f32_e32 v32, v29, v32
	v_add_f32_e32 v32, v34, v32
	v_add_f32_e32 v33, v35, v32
	v_sub_f32_e32 v32, v50, v67
	v_exp_f32_e32 v32, v32
	v_exp_f32_e32 v50, v49
	v_sub_f32_e32 v49, v98, v67
	v_exp_f32_e32 v55, v53
	v_add_f32_e32 v36, v32, v33
	v_sub_f32_e32 v33, v51, v67
	v_exp_f32_e32 v33, v33
	v_exp_f32_e32 v51, v49
	v_sub_f32_e32 v58, v58, v67
	v_exp_f32_e32 v58, v58
	v_add_f32_e32 v36, v33, v36
	v_add_f32_e32 v36, v38, v36
	v_add_f32_e32 v37, v39, v36
	v_sub_f32_e32 v36, v87, v67
	v_exp_f32_e32 v36, v36
	v_sub_f32_e32 v59, v59, v67
	v_exp_f32_e32 v59, v59
	v_sub_f32_e32 v56, v56, v67
	v_add_f32_e32 v40, v36, v37
	v_sub_f32_e32 v37, v88, v67
	v_exp_f32_e32 v37, v37
	v_exp_f32_e32 v56, v56
	v_sub_f32_e32 v57, v57, v67
	v_exp_f32_e32 v57, v57
	v_add_f32_e32 v40, v37, v40
	v_add_f32_e32 v40, v42, v40
	v_add_f32_e32 v41, v43, v40
	v_sub_f32_e32 v40, v91, v67
	v_exp_f32_e32 v40, v40
	v_sub_f32_e32 v62, v62, v67
	v_exp_f32_e32 v62, v62
	v_sub_f32_e32 v63, v63, v67
	v_add_f32_e32 v44, v40, v41
	v_sub_f32_e32 v41, v92, v67
	v_exp_f32_e32 v41, v41
	v_exp_f32_e32 v63, v63
	v_sub_f32_e32 v60, v60, v67
	v_exp_f32_e32 v60, v60
	v_add_f32_e32 v44, v41, v44
	v_add_f32_e32 v44, v46, v44
	v_add_f32_e32 v45, v47, v44
	v_sub_f32_e32 v44, v95, v67
	v_exp_f32_e32 v44, v44
	v_sub_f32_e32 v61, v61, v67
	v_exp_f32_e32 v61, v61
	v_sub_f32_e32 v69, v69, v67
	v_add_f32_e32 v48, v44, v45
	v_sub_f32_e32 v45, v96, v67
	v_exp_f32_e32 v45, v45
	v_sub_f32_e32 v66, v66, v67
	v_sub_f32_e32 v65, v65, v67
	v_sub_f32_e32 v64, v64, v67
	v_add_f32_e32 v48, v45, v48
	v_add_f32_e32 v48, v50, v48
	v_add_f32_e32 v49, v51, v48
	v_sub_f32_e32 v48, v99, v67
	v_exp_f32_e32 v48, v48
	s_nop 0
	v_add_f32_e32 v52, v48, v49
	v_sub_f32_e32 v49, v100, v67
	v_exp_f32_e32 v49, v49
	s_nop 0
	v_add_f32_e32 v52, v49, v52
	v_add_f32_e32 v52, v54, v52
	v_add_f32_e32 v53, v55, v52
	v_sub_f32_e32 v52, v103, v67
	v_exp_f32_e32 v52, v52
	s_nop 0
	v_add_f32_e32 v72, v52, v53
	v_sub_f32_e32 v53, v104, v67
	v_exp_f32_e32 v53, v53
	v_exp_f32_e32 v67, v64
	v_add_f32_e32 v72, v53, v72
	v_add_f32_e32 v72, v58, v72
	v_add_f32_e32 v72, v59, v72
	v_add_f32_e32 v72, v56, v72
	v_add_f32_e32 v72, v57, v72
	v_add_f32_e32 v72, v62, v72
	v_add_f32_e32 v72, v63, v72
	v_add_f32_e32 v72, v60, v72
	v_add_f32_e32 v73, v61, v72
	v_exp_f32_e32 v72, v69
	s_nop 0
	v_add_f32_e32 v69, v72, v73
	v_exp_f32_e32 v73, v66
	v_exp_f32_e32 v66, v65
	v_add_f32_e32 v69, v73, v69
	v_add_f32_e32 v65, v66, v69
	v_add_f32_e32 v64, v67, v65
	v_mov_b32_e32 v65, v64
	s_nop 1
	v_permlane32_swap_b32_e32 v64, v65
	v_add_f32_e32 v64, v64, v65
	v_div_scale_f32 v65, s[2:3], v64, v64, 1.0
	v_rcp_f32_e32 v69, v65
	v_cmp_lt_f32_e64 s[0:1], 0, v64
	v_fma_f32 v74, -v65, v69, 1.0
	v_fmac_f32_e32 v69, v74, v69
	v_div_scale_f32 v74, vcc, 1.0, v64, 1.0
	v_mul_f32_e32 v75, v74, v69
	v_fma_f32 v76, -v65, v75, v74
	v_fmac_f32_e32 v75, v76, v69
	v_fma_f32 v65, -v65, v75, v74
	v_div_fmas_f32 v65, v65, v69, v75
	v_and_b32_e32 v69, 64, v212
	v_div_fixup_f32 v64, v65, v64, 1.0
	v_xor_b32_e32 v65, 32, v212
	v_add_u32_e32 v69, 64, v69
	v_cmp_lt_i32_e32 vcc, v65, v69
	v_cndmask_b32_e64 v76, 0, v64, s[0:1]
	v_add_u32_e32 v64, s12, v71
	v_cndmask_b32_e32 v65, v212, v65, vcc
	v_lshlrev_b32_e32 v77, 2, v65
	v_pk_mul_f32 v[6:7], v[6:7], v[76:77] op_sel_hi:[1,0]
	ds_bpermute_b32 v74, v77, v7
	v_mul_lo_u32 v64, v64, s64
	v_lshlrev_b32_e32 v69, 2, v3
	v_add3_u32 v88, s33, v64, v69
	v_pk_mul_f32 v[64:65], v[4:5], v[76:77] op_sel_hi:[1,0]
	v_cmp_gt_u32_e32 vcc, 32, v68
	v_pk_mul_f32 v[4:5], v[70:71], v[64:65] op_sel_hi:[0,1]
	v_add_f32_e32 v75, v6, v7
	v_add_f32_e32 v64, v64, v65
	v_add_f32_e32 v64, v64, v75
	s_waitcnt lgkmcnt(0)
	v_cndmask_b32_e64 v65, v74, 0, vcc
	v_pk_mul_f32 v[8:9], v[8:9], v[76:77] op_sel_hi:[1,0]
	v_add_f32_e32 v64, v65, v64
	ds_bpermute_b32 v65, v77, v9
	v_pk_mul_f32 v[10:11], v[10:11], v[76:77] op_sel_hi:[1,0]
	v_add_f32_e32 v75, v8, v9
	v_pk_mul_f32 v[78:79], v[70:71], v[10:11] op_sel_hi:[0,1]
	v_add_f32_e32 v10, v10, v11
	v_add_f32_e32 v10, v10, v75
	s_waitcnt lgkmcnt(0)
	v_cndmask_b32_e32 v11, v65, v74, vcc
	v_add_f32_e32 v10, v11, v10
	ds_write2_b32 v88, v64, v10 offset1:2
	v_pk_mul_f32 v[10:11], v[12:13], v[76:77] op_sel_hi:[1,0]
	ds_bpermute_b32 v12, v77, v11
	v_add_f32_e32 v13, v10, v11
	v_pk_mul_f32 v[84:85], v[70:71], v[10:11] op_sel_hi:[0,1]
	v_pk_mul_f32 v[10:11], v[16:17], v[76:77] op_sel_hi:[1,0]
	v_pk_mul_f32 v[80:81], v[70:71], v[8:9] op_sel_hi:[0,1]
	v_pk_mul_f32 v[8:9], v[14:15], v[76:77] op_sel_hi:[1,0]
	ds_bpermute_b32 v14, v77, v11
	v_pk_mul_f32 v[82:83], v[70:71], v[8:9] op_sel_hi:[0,1]
	v_add_f32_e32 v8, v8, v9
	v_add_f32_e32 v8, v8, v13
	s_waitcnt lgkmcnt(1)
	v_cndmask_b32_e32 v9, v12, v65, vcc
	v_add_f32_e32 v13, v9, v8
	v_pk_mul_f32 v[8:9], v[18:19], v[76:77] op_sel_hi:[1,0]
	v_add_f32_e32 v15, v10, v11
	v_pk_mul_f32 v[86:87], v[70:71], v[10:11] op_sel_hi:[0,1]
	v_pk_mul_f32 v[10:11], v[20:21], v[76:77] op_sel_hi:[1,0]
	v_pk_mul_f32 v[18:19], v[70:71], v[8:9] op_sel_hi:[0,1]
	v_add_f32_e32 v8, v8, v9
	s_waitcnt lgkmcnt(0)
	v_cndmask_b32_e32 v9, v14, v12, vcc
	ds_bpermute_b32 v12, v77, v11
	v_add_f32_e32 v8, v8, v15
	v_add_f32_e32 v8, v9, v8
	ds_write2_b32 v88, v13, v8 offset0:4 offset1:6
	v_pk_mul_f32 v[8:9], v[22:23], v[76:77] op_sel_hi:[1,0]
	v_add_f32_e32 v13, v10, v11
	v_pk_mul_f32 v[20:21], v[70:71], v[10:11] op_sel_hi:[0,1]
	v_pk_mul_f32 v[10:11], v[24:25], v[76:77] op_sel_hi:[1,0]
	v_pk_mul_f32 v[22:23], v[70:71], v[8:9] op_sel_hi:[0,1]
	v_add_f32_e32 v8, v8, v9
	s_waitcnt lgkmcnt(1)
	v_cndmask_b32_e32 v9, v12, v14, vcc
	ds_bpermute_b32 v14, v77, v11
	v_add_f32_e32 v8, v8, v13
	v_add_f32_e32 v13, v8, v9
	v_pk_mul_f32 v[8:9], v[26:27], v[76:77] op_sel_hi:[1,0]
	v_add_f32_e32 v15, v10, v11
	v_pk_mul_f32 v[24:25], v[70:71], v[10:11] op_sel_hi:[0,1]
	v_pk_mul_f32 v[10:11], v[28:29], v[76:77] op_sel_hi:[1,0]
	v_pk_mul_f32 v[26:27], v[70:71], v[8:9] op_sel_hi:[0,1]
	v_add_f32_e32 v8, v8, v9
	s_waitcnt lgkmcnt(0)
	v_cndmask_b32_e32 v9, v14, v12, vcc
	ds_bpermute_b32 v12, v77, v11
	v_add_f32_e32 v8, v8, v15
	v_add_f32_e32 v8, v8, v9
	ds_write2_b32 v88, v13, v8 offset0:8 offset1:10
	v_pk_mul_f32 v[8:9], v[30:31], v[76:77] op_sel_hi:[1,0]
	v_add_f32_e32 v13, v10, v11
	v_pk_mul_f32 v[28:29], v[70:71], v[10:11] op_sel_hi:[0,1]
	v_pk_mul_f32 v[10:11], v[32:33], v[76:77] op_sel_hi:[1,0]
	v_pk_mul_f32 v[30:31], v[70:71], v[8:9] op_sel_hi:[0,1]
	v_add_f32_e32 v8, v8, v9
	s_waitcnt lgkmcnt(1)
	v_cndmask_b32_e32 v9, v12, v14, vcc
	ds_bpermute_b32 v14, v77, v11
	v_add_f32_e32 v8, v8, v13
	v_add_f32_e32 v13, v8, v9
	v_pk_mul_f32 v[8:9], v[34:35], v[76:77] op_sel_hi:[1,0]
	v_add_f32_e32 v15, v10, v11
	v_pk_mul_f32 v[34:35], v[70:71], v[8:9] op_sel_hi:[0,1]
	v_add_f32_e32 v8, v8, v9
	v_add_f32_e32 v8, v8, v15
	s_waitcnt lgkmcnt(0)
	v_cndmask_b32_e32 v9, v14, v12, vcc
	v_add_f32_e32 v8, v8, v9
	ds_write2_b32 v88, v13, v8 offset0:12 offset1:14
	v_pk_mul_f32 v[12:13], v[36:37], v[76:77] op_sel_hi:[1,0]
	ds_bpermute_b32 v36, v77, v13
	v_pk_mul_f32 v[16:17], v[40:41], v[76:77] op_sel_hi:[1,0]
	ds_bpermute_b32 v40, v77, v17
	v_pk_mul_f32 v[32:33], v[70:71], v[10:11] op_sel_hi:[0,1]
	v_pk_mul_f32 v[10:11], v[38:39], v[76:77] op_sel_hi:[1,0]
	v_add_f32_e32 v15, v12, v13
	v_pk_mul_f32 v[8:9], v[70:71], v[10:11] op_sel_hi:[0,1]
	v_add_f32_e32 v10, v10, v11
	v_add_f32_e32 v10, v10, v15
	s_waitcnt lgkmcnt(1)
	v_cndmask_b32_e32 v11, v36, v14, vcc
	v_pk_mul_f32 v[14:15], v[42:43], v[76:77] op_sel_hi:[1,0]
	v_add_f32_e32 v37, v10, v11
	v_pk_mul_f32 v[10:11], v[70:71], v[12:13] op_sel_hi:[0,1]
	v_pk_mul_f32 v[12:13], v[70:71], v[14:15] op_sel_hi:[0,1]
	v_add_f32_e32 v38, v16, v17
	v_add_f32_e32 v14, v14, v15
	v_add_f32_e32 v14, v14, v38
	s_waitcnt lgkmcnt(0)
	v_cndmask_b32_e32 v15, v40, v36, vcc
	v_pk_mul_f32 v[38:39], v[44:45], v[76:77] op_sel_hi:[1,0]
	v_add_f32_e32 v14, v14, v15
	ds_bpermute_b32 v41, v77, v39
	ds_write2_b32 v88, v37, v14 offset0:16 offset1:18
	v_pk_mul_f32 v[36:37], v[46:47], v[76:77] op_sel_hi:[1,0]
	v_pk_mul_f32 v[14:15], v[70:71], v[16:17] op_sel_hi:[0,1]
	v_pk_mul_f32 v[16:17], v[70:71], v[36:37] op_sel_hi:[0,1]
	v_add_f32_e32 v42, v38, v39
	v_add_f32_e32 v36, v36, v37
	v_pk_mul_f32 v[64:65], v[70:71], v[38:39] op_sel_hi:[0,1]
	v_pk_mul_f32 v[38:39], v[48:49], v[76:77] op_sel_hi:[1,0]
	v_add_f32_e32 v36, v36, v42
	ds_bpermute_b32 v42, v77, v39
	s_waitcnt lgkmcnt(2)
	v_cndmask_b32_e32 v37, v41, v40, vcc
	v_add_f32_e32 v40, v36, v37
	v_pk_mul_f32 v[36:37], v[50:51], v[76:77] op_sel_hi:[1,0]
	v_add_f32_e32 v43, v38, v39
	v_pk_mul_f32 v[50:51], v[70:71], v[36:37] op_sel_hi:[0,1]
	v_add_f32_e32 v36, v36, v37
	v_add_f32_e32 v36, v36, v43
	s_waitcnt lgkmcnt(0)
	v_cndmask_b32_e32 v37, v42, v41, vcc
	v_add_f32_e32 v36, v36, v37
	v_pk_mul_f32 v[74:75], v[70:71], v[38:39] op_sel_hi:[0,1]
	v_pk_mul_f32 v[38:39], v[52:53], v[76:77] op_sel_hi:[1,0]
	ds_write2_b32 v88, v40, v36 offset0:20 offset1:22
	ds_bpermute_b32 v40, v77, v39
	v_pk_mul_f32 v[36:37], v[54:55], v[76:77] op_sel_hi:[1,0]
	v_add_f32_e32 v41, v38, v39
	v_pk_mul_f32 v[52:53], v[70:71], v[38:39] op_sel_hi:[0,1]
	v_pk_mul_f32 v[38:39], v[56:57], v[76:77] op_sel_hi:[1,0]
	v_pk_mul_f32 v[54:55], v[70:71], v[36:37] op_sel_hi:[0,1]
	v_add_f32_e32 v36, v36, v37
	s_waitcnt lgkmcnt(0)
	v_cndmask_b32_e32 v37, v40, v42, vcc
	ds_bpermute_b32 v42, v77, v39
	v_add_f32_e32 v36, v36, v41
	v_add_f32_e32 v41, v36, v37
	v_pk_mul_f32 v[36:37], v[58:59], v[76:77] op_sel_hi:[1,0]
	v_add_f32_e32 v43, v38, v39
	v_pk_mul_f32 v[56:57], v[70:71], v[38:39] op_sel_hi:[0,1]
	v_pk_mul_f32 v[38:39], v[60:61], v[76:77] op_sel_hi:[1,0]
	v_pk_mul_f32 v[58:59], v[70:71], v[36:37] op_sel_hi:[0,1]
	v_add_f32_e32 v36, v36, v37
	s_waitcnt lgkmcnt(0)
	v_cndmask_b32_e32 v37, v42, v40, vcc
	ds_bpermute_b32 v40, v77, v39
	v_add_f32_e32 v36, v36, v43
	v_add_f32_e32 v36, v36, v37
	ds_write2_b32 v88, v41, v36 offset0:24 offset1:26
	v_pk_mul_f32 v[36:37], v[62:63], v[76:77] op_sel_hi:[1,0]
	v_add_f32_e32 v41, v38, v39
	v_pk_mul_f32 v[60:61], v[70:71], v[38:39] op_sel_hi:[0,1]
	v_pk_mul_f32 v[38:39], v[66:67], v[76:77] op_sel_hi:[1,0]
	v_pk_mul_f32 v[62:63], v[70:71], v[36:37] op_sel_hi:[0,1]
	v_add_f32_e32 v36, v36, v37
	s_waitcnt lgkmcnt(1)
	v_cndmask_b32_e32 v37, v40, v42, vcc
	ds_bpermute_b32 v42, v77, v39
	v_add_f32_e32 v36, v36, v41
	v_add_f32_e32 v41, v36, v37
	v_pk_mul_f32 v[36:37], v[72:73], v[76:77] op_sel_hi:[1,0]
	v_add_f32_e32 v43, v38, v39
	v_pk_mul_f32 v[72:73], v[70:71], v[36:37] op_sel_hi:[0,1]
	v_add_f32_e32 v36, v36, v37
	v_cvt_pk_bf16_f32 v78, v78, v79
	v_cvt_pk_bf16_f32 v79, v80, v81
	v_cvt_pk_bf16_f32 v80, v82, v83
	v_cvt_pk_bf16_f32 v82, v18, v19
	v_lshlrev_b32_e32 v18, 1, v68
	v_bfe_u32 v19, v68, 2, 2
	s_mov_b32 s0, 0x3fffffc
	v_add_f32_e32 v36, v36, v43
	s_waitcnt lgkmcnt(0)
	v_cndmask_b32_e32 v37, v42, v40, vcc
	v_and_b32_e32 v204, 32, v18
	v_and_or_b32 v19, v182, s0, v19
	v_add_f32_e32 v36, v36, v37
	v_add_u32_e32 v18, 0, v204
	v_lshlrev_b32_e32 v205, 6, v19
	v_pk_mul_f32 v[6:7], v[70:71], v[6:7] op_sel_hi:[0,1]
	ds_write2_b32 v88, v41, v36 offset0:28 offset1:30
	v_pk_mul_f32 v[66:67], v[70:71], v[38:39] op_sel_hi:[0,1]
	v_add3_u32 v70, v18, v201, v205
	v_add3_u32 v229, v18, v201, v205
	v_cvt_pk_bf16_f32 v81, v84, v85
	v_cvt_pk_bf16_f32 v83, v86, v87
	v_cvt_pk_bf16_f32 v84, v22, v23
	v_cvt_pk_bf16_f32 v85, v20, v21
	v_cvt_pk_bf16_f32 v87, v24, v25
	ds_read_b64_tr_b16 v[18:19], v70 offset:8192
	ds_read_b64_tr_b16 v[20:21], v70 offset:8704
	ds_read_b64_tr_b16 v[22:23], v70 offset:12288
	ds_read_b64_tr_b16 v[24:25], v70 offset:12800
	v_cvt_pk_bf16_f32 v76, v4, v5
	v_cvt_pk_bf16_f32 v77, v6, v7
	v_cvt_pk_bf16_f32 v86, v26, v27
	v_cvt_pk_bf16_f32 v4, v30, v31
	v_cvt_pk_bf16_f32 v5, v28, v29
	v_cvt_pk_bf16_f32 v6, v34, v35
	v_cvt_pk_bf16_f32 v7, v32, v33
	s_waitcnt lgkmcnt(2)
	v_mfma_f32_32x32x16_bf16 v[34:49], v[18:21], v[76:79], 0
	s_waitcnt lgkmcnt(0)
	v_mfma_f32_32x32x16_bf16 v[18:33], v[22:25], v[76:79], 0
	ds_read_b64_tr_b16 v[76:77], v70 offset:9216
	ds_read_b64_tr_b16 v[78:79], v70 offset:9728
	ds_read_b64_tr_b16 v[88:89], v70 offset:13312
	ds_read_b64_tr_b16 v[90:91], v70 offset:13824
	s_waitcnt lgkmcnt(2)
	v_mfma_f32_32x32x16_bf16 v[34:49], v[76:79], v[80:83], v[34:49]
	s_waitcnt lgkmcnt(0)
	v_mfma_f32_32x32x16_bf16 v[18:33], v[88:91], v[80:83], v[18:33]
	ds_read_b64_tr_b16 v[76:77], v70 offset:10240
	ds_read_b64_tr_b16 v[78:79], v70 offset:10752
	ds_read_b64_tr_b16 v[80:81], v70 offset:14336
	ds_read_b64_tr_b16 v[82:83], v70 offset:14848
	s_waitcnt lgkmcnt(2)
	v_mfma_f32_32x32x16_bf16 v[34:49], v[76:79], v[84:87], v[34:49]
	s_waitcnt lgkmcnt(0)
	v_mfma_f32_32x32x16_bf16 v[18:33], v[80:83], v[84:87], v[18:33]
	ds_read_b64_tr_b16 v[76:77], v70 offset:11264
	ds_read_b64_tr_b16 v[78:79], v70 offset:11776
	ds_read_b64_tr_b16 v[80:81], v70 offset:15360
	ds_read_b64_tr_b16 v[82:83], v70 offset:15872
	s_waitcnt lgkmcnt(2)
	v_mfma_f32_32x32x16_bf16 v[34:49], v[76:79], v[4:7], v[34:49]
	v_cvt_pk_bf16_f32 v76, v8, v9
	v_cvt_pk_bf16_f32 v77, v10, v11
	v_cvt_pk_bf16_f32 v79, v14, v15
	v_cvt_pk_bf16_f32 v14, v50, v51
	v_cvt_pk_bf16_f32 v8, v54, v55
	v_cvt_pk_bf16_f32 v9, v52, v53
	v_cvt_pk_bf16_f32 v11, v56, v57
	s_waitcnt lgkmcnt(0)
	v_mfma_f32_32x32x16_bf16 v[18:33], v[80:83], v[4:7], v[18:33]
	ds_read_b64_tr_b16 v[50:51], v70 offset:24576
	ds_read_b64_tr_b16 v[52:53], v70 offset:25088
	ds_read_b64_tr_b16 v[54:55], v70 offset:28672
	ds_read_b64_tr_b16 v[56:57], v70 offset:29184
	v_cvt_pk_bf16_f32 v78, v12, v13
	v_cvt_pk_bf16_f32 v12, v16, v17
	v_cvt_pk_bf16_f32 v13, v64, v65
	v_cvt_pk_bf16_f32 v15, v74, v75
	v_cvt_pk_bf16_f32 v10, v58, v59
	v_cvt_pk_bf16_f32 v4, v62, v63
	s_waitcnt lgkmcnt(2)
	v_mfma_f32_32x32x16_bf16 v[34:49], v[50:53], v[76:79], v[34:49]
	v_cvt_pk_bf16_f32 v5, v60, v61
	v_cvt_pk_bf16_f32 v6, v72, v73
	v_cvt_pk_bf16_f32 v7, v66, v67
	s_waitcnt lgkmcnt(0)
	v_mfma_f32_32x32x16_bf16 v[18:33], v[54:57], v[76:79], v[18:33]
	ds_read_b64_tr_b16 v[50:51], v70 offset:25600
	ds_read_b64_tr_b16 v[52:53], v70 offset:26112
	ds_read_b64_tr_b16 v[54:55], v70 offset:29696
	ds_read_b64_tr_b16 v[56:57], v70 offset:30208
	s_waitcnt lgkmcnt(2)
	v_mfma_f32_32x32x16_bf16 v[34:49], v[50:53], v[12:15], v[34:49]
	s_waitcnt lgkmcnt(0)
	v_mfma_f32_32x32x16_bf16 v[18:33], v[54:57], v[12:15], v[18:33]
	ds_read_b64_tr_b16 v[12:13], v70 offset:26624
	ds_read_b64_tr_b16 v[14:15], v70 offset:27136
	ds_read_b64_tr_b16 v[50:51], v70 offset:30720
	ds_read_b64_tr_b16 v[52:53], v70 offset:31232
	s_waitcnt lgkmcnt(2)
	v_mfma_f32_32x32x16_bf16 v[34:49], v[12:15], v[8:11], v[34:49]
	s_waitcnt lgkmcnt(0)
	v_mfma_f32_32x32x16_bf16 v[18:33], v[50:53], v[8:11], v[18:33]
	ds_read_b64_tr_b16 v[8:9], v70 offset:27648
	ds_read_b64_tr_b16 v[10:11], v70 offset:28160
	ds_read_b64_tr_b16 v[12:13], v70 offset:31744
	ds_read_b64_tr_b16 v[14:15], v70 offset:32256
	s_waitcnt lgkmcnt(2)
	v_mfma_f32_32x32x16_bf16 v[34:49], v[8:11], v[4:7], v[34:49]
	s_waitcnt lgkmcnt(0)
	v_mfma_f32_32x32x16_bf16 v[18:33], v[12:15], v[4:7], v[18:33]
	s_cbranch_scc1 .LBB0_640
	s_cmp_gt_u32 s78, 7
	s_cselect_b64 s[94:95], -1, 0
	s_cmp_gt_u32 s82, 3
	s_cselect_b64 s[96:97], -1, 0
	s_sub_i32 s0, 3, s80
	s_mov_b32 s1, s16
	s_lshl_b64 s[0:1], s[0:1], 13
	v_readlane_b32 s9, v251, 59
	s_add_u32 s2, s9, s0
	v_readlane_b32 s10, v251, 61
	s_addc_u32 s3, s10, s1
	s_add_i32 s0, s79, 4
	s_mov_b32 s1, s16
	s_lshl_b64 s[0:1], s[0:1], 13
	v_writelane_b32 v249, s40, 10
	s_add_u32 s7, s92, s0
	s_mov_b32 s12, s16
	s_addc_u32 s8, s93, s1
	s_mov_b32 s1, s16
	v_writelane_b32 v249, s12, 11
	s_cmp_gt_u32 s82, 4
	s_cselect_b64 s[4:5], -1, 0
	v_writelane_b32 v249, s13, 12
	s_sub_i32 s0, 4, s80
	v_writelane_b32 v249, s14, 13
	s_lshl_b64 s[0:1], s[0:1], 13
	v_writelane_b32 v249, s15, 14
	s_add_u32 s9, s9, s0
	v_writelane_b32 v249, s16, 15
	s_addc_u32 s10, s10, s1
	s_add_i32 s0, s79, 5
	v_writelane_b32 v249, s17, 16
	s_mov_b32 s1, s16
	v_writelane_b32 v249, s18, 17
	s_lshl_b64 s[0:1], s[0:1], 13
	v_writelane_b32 v249, s19, 18
	s_add_u32 s0, s92, s0
	v_writelane_b32 v249, s20, 19
	s_addc_u32 s1, s93, s1
	s_sub_i32 s11, 30, s6
	v_writelane_b32 v249, s21, 20
	s_cmp_gt_i32 s80, 3
	v_writelane_b32 v249, s22, 21
	s_cselect_b32 s2, s7, s2
	v_writelane_b32 v249, s23, 22
	s_cselect_b32 s3, s8, s3
	s_add_u32 s2, s2, s90
	v_writelane_b32 v249, s24, 23
	s_addc_u32 s3, s3, s91
	v_writelane_b32 v249, s25, 24
	s_cmp_gt_i32 s80, 4
	v_writelane_b32 v249, s26, 25
	s_cselect_b32 s0, s0, s9
	v_writelane_b32 v249, s27, 26
	s_cselect_b32 s1, s1, s10
	s_add_u32 s12, s0, s90
	s_addc_u32 s13, s1, s91
	v_cmp_eq_u32_e32 vcc, 0, v198
	v_cmp_eq_u32_e64 s[0:1], s78, v198
	s_or_b64 s[0:1], vcc, s[0:1]
	v_cmp_eq_u32_e32 vcc, s11, v198
	s_or_b64 s[8:9], s[0:1], vcc
	v_readlane_b32 s0, v250, 44
	v_and_b32_e32 v4, 0x3fffffe0, v68
	v_lshl_add_u64 v[186:187], s[2:3], 0, v[184:185]
	v_lshl_add_u32 v206, v68, 2, s0
	v_lshl_add_u32 v207, v4, 2, s0
	s_mov_b64 s[0:1], 0x800000
	v_lshl_add_u64 v[190:191], s[12:13], 0, v[184:185]
	v_sub_u32_e32 v208, v71, v69
	v_lshl_add_u64 v[188:189], v[186:187], 0, s[0:1]
	v_lshl_add_u64 v[192:193], v[190:191], 0, s[0:1]
	v_mul_lo_u32 v3, v3, s64
	v_lshlrev_b32_e32 v4, 2, v198
	v_readlane_b32 s0, v250, 47
	v_lshlrev_b32_e32 v50, 2, v71
	v_mov_b32_e32 v16, v2
	v_add3_u32 v209, s0, v3, v4
	v_cmp_gt_i32_e64 s[0:1], 1, v208
	v_mov_b32_e32 v17, v2
	s_sub_i32 s83, s80, s6
	v_writelane_b32 v249, s0, 27
	v_mov_b32_e32 v3, v2
	v_mov_b32_e32 v4, v2
	v_writelane_b32 v249, s1, 28
	v_cmp_gt_i32_e64 s[0:1], 0, v208
	v_mov_b32_e32 v5, v2
	v_mov_b32_e32 v6, v2
	v_writelane_b32 v249, s0, 29
	v_mov_b32_e32 v7, v2
	v_mov_b32_e32 v8, v2
	v_writelane_b32 v249, s1, 30
	v_cmp_gt_i32_e64 s[0:1], 33, v208
	v_mov_b32_e32 v9, v2
	v_mov_b32_e32 v10, v2
	v_writelane_b32 v249, s0, 31
	v_mov_b32_e32 v11, v2
	v_mov_b32_e32 v12, v2
	v_writelane_b32 v249, s1, 32
	v_cmp_gt_i32_e64 s[0:1], 32, v208
	v_mov_b32_e32 v13, v2
	v_mov_b32_e32 v14, v2
	v_writelane_b32 v249, s0, 33
	v_mov_b32_e32 v15, v2
	v_add_u32_e32 v50, 0, v50
	v_writelane_b32 v249, s1, 34
	v_cmp_gt_i32_e64 s[0:1], 3, v208
	v_mov_b64_e32 v[96:97], v[16:17]
	v_mov_b64_e32 v[112:113], v[16:17]
	v_writelane_b32 v249, s0, 35
	s_add_i32 s83, s83, 32
	v_cmp_lt_u32_e64 s[6:7], s78, v198
	v_writelane_b32 v249, s1, 36
	v_cmp_gt_i32_e64 s[0:1], 2, v208
	v_mov_b32_e32 v211, 0
	v_cmp_eq_u32_e64 s[10:11], 0, v68
	v_writelane_b32 v249, s0, 37
	v_cmp_ne_u32_e64 s[12:13], 0, v198
	v_cmp_lt_u32_e64 s[14:15], 1, v198
	v_writelane_b32 v249, s1, 38
	v_cmp_gt_i32_e64 s[0:1], 35, v208
	v_cmp_lt_u32_e64 s[16:17], 2, v198
	v_cmp_lt_u32_e64 s[18:19], 3, v198
	v_writelane_b32 v249, s0, 39
	v_cmp_lt_u32_e64 s[20:21], 4, v198
	v_cmp_lt_u32_e64 s[22:23], 5, v198
	v_writelane_b32 v249, s1, 40
	v_cmp_gt_i32_e64 s[0:1], 34, v208
	v_cmp_lt_u32_e64 s[24:25], 6, v198
	v_cmp_lt_u32_e64 s[26:27], 7, v198
	v_writelane_b32 v249, s0, 41
	v_cmp_lt_u32_e64 s[28:29], 8, v198
	v_cmp_lt_u32_e64 s[30:31], 9, v198
	v_writelane_b32 v249, s1, 42
	v_cmp_gt_i32_e64 s[0:1], 9, v208
	v_cmp_lt_u32_e64 s[34:35], 10, v198
	v_cmp_lt_u32_e64 s[36:37], 11, v198
	v_writelane_b32 v249, s0, 43
	v_cmp_lt_u32_e64 s[38:39], 12, v198
	v_cmp_lt_u32_e64 s[40:41], 13, v198
	v_writelane_b32 v249, s1, 44
	v_cmp_gt_i32_e64 s[0:1], 8, v208
	v_cmp_lt_u32_e64 s[42:43], 14, v198
	v_cmp_lt_u32_e64 s[44:45], 15, v198
	v_writelane_b32 v249, s0, 45
	v_cmp_lt_u32_e64 s[46:47], 16, v198
	v_cmp_lt_u32_e64 s[48:49], 17, v198
	v_writelane_b32 v249, s1, 46
	v_cmp_gt_i32_e64 s[0:1], 41, v208
	v_cmp_lt_u32_e64 s[50:51], 18, v198
	v_cmp_lt_u32_e64 s[52:53], 19, v198
	v_writelane_b32 v249, s0, 47
	v_cmp_lt_u32_e64 s[54:55], 20, v198
	v_cmp_lt_u32_e64 s[56:57], 21, v198
	v_writelane_b32 v249, s1, 48
	v_cmp_gt_i32_e64 s[0:1], 40, v208
	v_cmp_lt_u32_e64 s[58:59], 22, v198
	v_cmp_lt_u32_e64 s[60:61], 23, v198
	v_writelane_b32 v249, s0, 49
	v_cmp_lt_u32_e64 s[62:63], 24, v198
	s_mov_b32 s2, 0
	v_writelane_b32 v249, s1, 50
	v_cmp_gt_i32_e64 s[0:1], 11, v208
	v_mov_b32_e32 v214, 0
	v_add_u32_e32 v210, 0x20400, v50
	v_writelane_b32 v249, s0, 51
	v_mov_b32_e32 v114, 0
	v_mov_b64_e32 v[94:95], v[14:15]
	v_writelane_b32 v249, s1, 52
	v_cmp_gt_i32_e64 s[0:1], 10, v208
	v_mov_b64_e32 v[92:93], v[12:13]
	v_mov_b64_e32 v[90:91], v[10:11]
	v_writelane_b32 v249, s0, 53
	v_mov_b64_e32 v[88:89], v[8:9]
	v_mov_b64_e32 v[86:87], v[6:7]
	v_writelane_b32 v249, s1, 54
	v_cmp_gt_i32_e64 s[0:1], 43, v208
	v_mov_b64_e32 v[84:85], v[4:5]
	v_mov_b64_e32 v[82:83], v[2:3]
	v_writelane_b32 v249, s0, 55
	v_mov_b64_e32 v[110:111], v[14:15]
	v_mov_b64_e32 v[108:109], v[12:13]
	v_writelane_b32 v249, s1, 56
	v_cmp_gt_i32_e64 s[0:1], 42, v208
	v_mov_b64_e32 v[106:107], v[10:11]
	v_mov_b64_e32 v[104:105], v[8:9]
	v_writelane_b32 v249, s0, 57
	v_mov_b64_e32 v[102:103], v[6:7]
	v_mov_b64_e32 v[100:101], v[4:5]
	v_writelane_b32 v249, s1, 58
	v_cmp_gt_i32_e64 s[0:1], 17, v208
	v_mov_b64_e32 v[98:99], v[2:3]
	v_cmp_lt_u32_e64 s[64:65], 25, v198
	v_writelane_b32 v249, s0, 59
	v_cmp_lt_u32_e64 s[66:67], 26, v198
	v_cmp_lt_u32_e64 s[68:69], 27, v198
	v_writelane_b32 v249, s1, 60
	v_cmp_gt_i32_e64 s[0:1], 16, v208
	v_cmp_lt_u32_e64 s[70:71], 28, v198
	v_cmp_lt_u32_e64 s[72:73], 29, v198
	v_writelane_b32 v249, s0, 61
	v_cmp_eq_u32_e64 s[74:75], 31, v198
	s_nop 0
	v_writelane_b32 v249, s1, 62
	v_cmp_gt_i32_e64 s[0:1], 49, v208
	s_nop 1
	v_writelane_b32 v249, s0, 63
	s_nop 1
	v_writelane_b32 v248, s1, 0
	v_cmp_gt_i32_e64 s[0:1], 48, v208
	s_nop 1
	v_writelane_b32 v248, s0, 1
	s_nop 1
	v_writelane_b32 v248, s1, 2
	v_cmp_gt_i32_e64 s[0:1], 19, v208
	s_nop 1
	v_writelane_b32 v248, s0, 3
	s_nop 1
	v_writelane_b32 v248, s1, 4
	v_cmp_gt_i32_e64 s[0:1], 18, v208
	s_nop 1
	v_writelane_b32 v248, s0, 5
	s_nop 1
	v_writelane_b32 v248, s1, 6
	v_cmp_gt_i32_e64 s[0:1], 51, v208
	s_nop 1
	v_writelane_b32 v248, s0, 7
	s_nop 1
	v_writelane_b32 v248, s1, 8
	v_cmp_gt_i32_e64 s[0:1], 50, v208
	s_nop 1
	v_writelane_b32 v248, s0, 9
	s_nop 1
	v_writelane_b32 v248, s1, 10
	v_cmp_gt_i32_e64 s[0:1], 25, v208
	s_nop 1
	v_writelane_b32 v248, s0, 11
	s_nop 1
	v_writelane_b32 v248, s1, 12
	v_cmp_gt_i32_e64 s[0:1], 24, v208
	s_nop 1
	v_writelane_b32 v248, s0, 13
	s_nop 1
	v_writelane_b32 v248, s1, 14
	v_cmp_gt_i32_e64 s[0:1], 57, v208
	s_nop 1
	v_writelane_b32 v248, s0, 15
	s_nop 1
	v_writelane_b32 v248, s1, 16
	v_cmp_gt_i32_e64 s[0:1], 56, v208
	s_nop 1
	v_writelane_b32 v248, s0, 17
	s_nop 1
	v_writelane_b32 v248, s1, 18
	v_cmp_gt_i32_e64 s[0:1], 27, v208
	s_nop 1
	v_writelane_b32 v248, s0, 19
	s_nop 1
	v_writelane_b32 v248, s1, 20
	v_cmp_gt_i32_e64 s[0:1], 26, v208
	s_nop 1
	v_writelane_b32 v248, s0, 21
	s_nop 1
	v_writelane_b32 v248, s1, 22
	v_cmp_gt_i32_e64 s[0:1], 59, v208
	s_nop 1
	v_writelane_b32 v248, s0, 23
	s_nop 1
	v_writelane_b32 v248, s1, 24
	v_cmp_gt_i32_e64 s[0:1], 58, v208
	s_nop 1
	v_writelane_b32 v248, s0, 25
	s_nop 1
	v_writelane_b32 v248, s1, 26
	v_mov_b64_e32 v[50:51], 0
	v_mov_b64_e32 v[52:53], 0
	v_mov_b64_e32 v[54:55], 0
	v_mov_b64_e32 v[56:57], 0
	v_mov_b64_e32 v[58:59], 0
	v_mov_b64_e32 v[60:61], 0
	v_mov_b64_e32 v[62:63], 0
	v_mov_b64_e32 v[64:65], 0
	v_mov_b64_e32 v[66:67], 0
	v_mov_b64_e32 v[68:69], 0
	v_mov_b64_e32 v[70:71], 0
	v_mov_b64_e32 v[72:73], 0
	v_mov_b64_e32 v[74:75], 0
	v_mov_b64_e32 v[76:77], 0
	v_mov_b64_e32 v[78:79], 0
	v_mov_b64_e32 v[80:81], 0
	s_mov_b32 s32, 0x8000
	v_readlane_b32 s98, v251, 57
	s_add_i32 s99, s82, -5
	s_max_i32 s99, s99, 0
	s_cmp_gt_i32 s80, 5
	s_cbranch_scc1 .Lnsa_e6_win
	s_sub_i32 s0, 5, s80
	s_lshl_b32 s0, s0, 13
	v_readlane_b32 s100, v251, 59
	v_readlane_b32 s101, v251, 61
	s_branch .Lnsa_e6_done

.LBB0_574:
	s_add_i32 s0, s2, -1
	s_cmp_lt_u32 s0, s99
	s_cbranch_scc0 .Lnsa_step_general
	s_waitcnt vmcnt(8) lgkmcnt(0)
	s_barrier
	s_mov_b64 s[86:87], 0
	v_lshl_add_u64 v[4:5], s[100:101], 0, v[184:185]
	s_sub_i32 s3, s32, 0x4000
	s_cmp_lt_i32 s3, 0
	s_cselect_b32 s3, 0x14000, s3
	s_mov_b64 s[0:1], 0x800000
	s_add_i32 m0, s98, s3
	s_add_u32 s100, s100, 0x2000
	s_addc_u32 s101, s101, 0
	global_load_lds_dwordx4 v[4:5], off
	v_lshl_add_u64 v[4:5], v[4:5], 0, s[0:1]
	s_add_i32 m0, m0, 0x2000
	s_add_i32 s0, s2, 5
	s_cmp_lg_u32 s0, s80
	global_load_lds_dwordx4 v[4:5], off
	s_cbranch_scc1 .LBB0_599
	v_readlane_b32 s100, v251, 59
	v_readlane_b32 s101, v251, 61
	s_add_u32 s100, s100, s90
	s_addc_u32 s101, s101, s91
	s_branch .LBB0_599
